# grid barrier: waiting workgroups poll the top generation word directly (one hop less), per-XCD generation add dropped
# speedup vs baseline: 1.0051x; 1.0051x over previous
; __device__ __forceinline__ unsigned xb_add(unsigned* p, unsigned v) { return __hip_atomic_fetch_add(p, v, __ATOMIC_RELAXED, __HIP_MEMORY_SCOPE_AGENT); }
; template <class Idle>
; __device__ __forceinline__ void xcd_barrier(const XcdBarrier& b, Idle&& idle) {
;     ...
;             __builtin_amdgcn_fence(__ATOMIC_ACQUIRE, "agent");
;             xb_add(&bar[XB_XGEN(b.x)], 1u);
;             asm volatile("s_waitcnt vmcnt(0)" ::: "memory");
;             b.st[2] = 1u;
.LBB0_92:
	s_or_b64 exec, exec, s[6:7]
	s_mov_b64 s[6:7], exec
	v_mbcnt_lo_u32_b32 v1, s6, 0
	v_mbcnt_hi_u32_b32 v1, s7, v1
	v_cmp_eq_u32_e32 vcc, 0, v1
	s_waitcnt vmcnt(0)
	buffer_inv sc1
	s_and_saveexec_b64 s[8:9], vcc
	s_cbranch_execz .LBB0_94
	s_bcnt1_i32_b64 s2, s[6:7]
	v_mov_b32_e32 v1, 0x2000
	v_mov_b32_e32 v2, s2
.LBB0_94:
	s_or_b64 exec, exec, s[8:9]
	s_waitcnt vmcnt(0)
	s_add_i32 s2, 0, 0x27ff8
	v_mov_b32_e32 v1, 1
	v_mov_b32_e32 v2, s2
	ds_write_b32 v2, v1

; __device__ __forceinline__ unsigned xb_ld(unsigned* p)              { return __hip_atomic_load(p, __ATOMIC_RELAXED, __HIP_MEMORY_SCOPE_AGENT); }
; #define XB_SPIN(cond, bar) do { unsigned _sp = 0; while (cond) { __builtin_amdgcn_s_sleep(1); \
;     if ((++_sp & 255u) == 0u) { if (xb_ld(&(bar)[XB_TMO])) break; if (_sp > XB_SPIN_CAP) { atomicAdd(&(bar)[XB_TMO], 1u); break; } } } } while (0)
; template <class Idle>
; __device__ __forceinline__ void xcd_barrier(const XcdBarrier& b, Idle&& idle) {
;     ...
;         if (threadIdx.x == 0) {
;             unsigned* bar = b.bar; const unsigned gen = b.st[3];
;             bool rel = xb_ld(&bar[XB_XGEN(b.x)]) != gen;
;             if (!rel && anyw == 0ull) { XB_SPIN(xb_ld(&bar[XB_XGEN(b.x)]) == gen, bar); rel = true; }
;             if (!rel && ++rounds > (1u << 16)) { atomicAdd(&bar[XB_TMO], 1u); rel = true; }
;             if (rel) { __builtin_amdgcn_fence(__ATOMIC_ACQUIRE, "agent"); asm volatile("s_waitcnt vmcnt(0)" ::: "memory"); b.st[2] = 1u; }
.LBB0_116:
	s_lshl_b32 s0, s97, 8
	s_add_u32 s0, s74, s0
	s_addc_u32 s1, s75, 0
	s_add_u32 s0, s74, 0x3500
	s_addc_u32 s1, s75, 0
	s_add_i32 s12, 0, 0x27ffc
	v_mov_b32_e32 v1, 0
	v_mov_b32_e32 v2, 1
	v_mov_b32_e32 v3, s3
	s_branch .LBB0_120

; __device__ __forceinline__ unsigned xb_add(unsigned* p, unsigned v) { return __hip_atomic_fetch_add(p, v, __ATOMIC_RELAXED, __HIP_MEMORY_SCOPE_AGENT); }
; template <class Idle>
; __device__ __forceinline__ void xcd_barrier(const XcdBarrier& b, Idle&& idle) {
;     ...
;             __builtin_amdgcn_fence(__ATOMIC_ACQUIRE, "agent");
;             xb_add(&bar[XB_XGEN(b.x)], 1u);
;             asm volatile("s_waitcnt vmcnt(0)" ::: "memory");
;             b.st[2] = 1u;
.LBB0_160:
	s_or_b64 exec, exec, s[6:7]
	s_mov_b64 s[6:7], exec
	v_mbcnt_lo_u32_b32 v1, s6, 0
	v_mbcnt_hi_u32_b32 v1, s7, v1
	v_cmp_eq_u32_e32 vcc, 0, v1
	s_waitcnt vmcnt(0)
	buffer_inv sc1
	s_and_saveexec_b64 s[8:9], vcc
	s_cbranch_execz .LBB0_162
	s_bcnt1_i32_b64 s2, s[6:7]
	v_mov_b32_e32 v1, 0x2000
	v_mov_b32_e32 v2, s2
.LBB0_162:
	s_or_b64 exec, exec, s[8:9]
	s_waitcnt vmcnt(0)
	s_add_i32 s2, 0, 0x27ff8
	v_mov_b32_e32 v1, 1
	v_mov_b32_e32 v2, s2
	ds_write_b32 v2, v1

; __device__ __forceinline__ unsigned xb_add(unsigned* p, unsigned v) { return __hip_atomic_fetch_add(p, v, __ATOMIC_RELAXED, __HIP_MEMORY_SCOPE_AGENT); }
; template <class Idle>
; __device__ __forceinline__ void xcd_barrier(const XcdBarrier& b, Idle&& idle) {
;     ...
;             __builtin_amdgcn_fence(__ATOMIC_ACQUIRE, "agent");
;             xb_add(&bar[XB_XGEN(b.x)], 1u);
;             asm volatile("s_waitcnt vmcnt(0)" ::: "memory");
;             b.st[2] = 1u;
.LBB0_248:
	s_or_b64 exec, exec, s[6:7]
	s_mov_b64 s[6:7], exec
	v_mbcnt_lo_u32_b32 v1, s6, 0
	v_mbcnt_hi_u32_b32 v1, s7, v1
	v_cmp_eq_u32_e32 vcc, 0, v1
	s_waitcnt vmcnt(0)
	buffer_inv sc1
	s_and_saveexec_b64 s[8:9], vcc
	s_cbranch_execz .LBB0_250
	s_bcnt1_i32_b64 s2, s[6:7]
	v_mov_b32_e32 v1, 0x2000
	v_mov_b32_e32 v2, s2
.LBB0_250:
	s_or_b64 exec, exec, s[8:9]
	s_waitcnt vmcnt(0)
	s_add_i32 s2, 0, 0x27ff8
	v_mov_b32_e32 v1, 1
	v_mov_b32_e32 v2, s2
	ds_write_b32 v2, v1

; __device__ __forceinline__ unsigned xb_add(unsigned* p, unsigned v) { return __hip_atomic_fetch_add(p, v, __ATOMIC_RELAXED, __HIP_MEMORY_SCOPE_AGENT); }
; template <class Idle>
; __device__ __forceinline__ void xcd_barrier(const XcdBarrier& b, Idle&& idle) {
;     ...
;             __builtin_amdgcn_fence(__ATOMIC_ACQUIRE, "agent");
;             xb_add(&bar[XB_XGEN(b.x)], 1u);
;             asm volatile("s_waitcnt vmcnt(0)" ::: "memory");
;             b.st[2] = 1u;
.LBB0_343:
	s_or_b64 exec, exec, s[6:7]
	s_mov_b64 s[6:7], exec
	v_mbcnt_lo_u32_b32 v1, s6, 0
	v_mbcnt_hi_u32_b32 v1, s7, v1
	v_cmp_eq_u32_e32 vcc, 0, v1
	s_waitcnt vmcnt(0)
	buffer_inv sc1
	s_and_saveexec_b64 s[8:9], vcc
	s_cbranch_execz .LBB0_345
	s_bcnt1_i32_b64 s2, s[6:7]
	v_mov_b32_e32 v1, 0x2000
	v_mov_b32_e32 v2, s2
.LBB0_345:
	s_or_b64 exec, exec, s[8:9]
	s_waitcnt vmcnt(0)
	s_add_i32 s2, 0, 0x27ff8
	v_mov_b32_e32 v1, 1
	v_mov_b32_e32 v2, s2
	ds_write_b32 v2, v1

; __device__ __forceinline__ unsigned xb_add(unsigned* p, unsigned v) { return __hip_atomic_fetch_add(p, v, __ATOMIC_RELAXED, __HIP_MEMORY_SCOPE_AGENT); }
; template <class Idle>
; __device__ __forceinline__ void xcd_barrier(const XcdBarrier& b, Idle&& idle) {
;     ...
;             __builtin_amdgcn_fence(__ATOMIC_ACQUIRE, "agent");
;             xb_add(&bar[XB_XGEN(b.x)], 1u);
;             asm volatile("s_waitcnt vmcnt(0)" ::: "memory");
;             b.st[2] = 1u;
.LBB0_422:
	s_or_b64 exec, exec, s[6:7]
	s_mov_b64 s[6:7], exec
	v_mbcnt_lo_u32_b32 v1, s6, 0
	v_mbcnt_hi_u32_b32 v1, s7, v1
	v_cmp_eq_u32_e32 vcc, 0, v1
	s_waitcnt vmcnt(0)
	buffer_inv sc1
	s_and_saveexec_b64 s[8:9], vcc
	s_cbranch_execz .LBB0_424
	s_bcnt1_i32_b64 s2, s[6:7]
	v_mov_b32_e32 v1, 0x2000
	v_mov_b32_e32 v2, s2
.LBB0_424:
	s_or_b64 exec, exec, s[8:9]
	s_waitcnt vmcnt(0)
	s_add_i32 s2, 0, 0x27ff8
	v_mov_b32_e32 v1, 1
	v_mov_b32_e32 v2, s2
	ds_write_b32 v2, v1

; __device__ __forceinline__ unsigned xb_add(unsigned* p, unsigned v) { return __hip_atomic_fetch_add(p, v, __ATOMIC_RELAXED, __HIP_MEMORY_SCOPE_AGENT); }
; template <class Idle>
; __device__ __forceinline__ void xcd_barrier(const XcdBarrier& b, Idle&& idle) {
;     ...
;             __builtin_amdgcn_fence(__ATOMIC_ACQUIRE, "agent");
;             xb_add(&bar[XB_XGEN(b.x)], 1u);
;             asm volatile("s_waitcnt vmcnt(0)" ::: "memory");
;             b.st[2] = 1u;
.LBB0_568:
	s_or_b64 exec, exec, s[6:7]
	s_mov_b64 s[6:7], exec
	v_mbcnt_lo_u32_b32 v1, s6, 0
	v_mbcnt_hi_u32_b32 v1, s7, v1
	v_cmp_eq_u32_e32 vcc, 0, v1
	s_waitcnt vmcnt(0)
	buffer_inv sc1
	s_and_saveexec_b64 s[8:9], vcc
	s_cbranch_execz .LBB0_570
	s_bcnt1_i32_b64 s2, s[6:7]
	v_mov_b32_e32 v1, 0x2000
	v_mov_b32_e32 v2, s2
.LBB0_570:
	s_or_b64 exec, exec, s[8:9]
	s_waitcnt vmcnt(0)
	s_add_i32 s2, 0, 0x27ff8
	v_mov_b32_e32 v1, 1
	v_mov_b32_e32 v2, s2
	ds_write_b32 v2, v1

; __device__ __forceinline__ unsigned xb_add(unsigned* p, unsigned v) { return __hip_atomic_fetch_add(p, v, __ATOMIC_RELAXED, __HIP_MEMORY_SCOPE_AGENT); }
; template <class Idle>
; __device__ __forceinline__ void xcd_barrier(const XcdBarrier& b, Idle&& idle) {
;     ...
;             __builtin_amdgcn_fence(__ATOMIC_ACQUIRE, "agent");
;             xb_add(&bar[XB_XGEN(b.x)], 1u);
;             asm volatile("s_waitcnt vmcnt(0)" ::: "memory");
;             b.st[2] = 1u;
.LBB0_649:
	s_or_b64 exec, exec, s[6:7]
	s_mov_b64 s[6:7], exec
	v_mbcnt_lo_u32_b32 v1, s6, 0
	v_mbcnt_hi_u32_b32 v1, s7, v1
	v_cmp_eq_u32_e32 vcc, 0, v1
	s_waitcnt vmcnt(0)
	buffer_inv sc1
	s_and_saveexec_b64 s[8:9], vcc
	s_cbranch_execz .LBB0_651
	s_bcnt1_i32_b64 s2, s[6:7]
	v_mov_b32_e32 v1, 0x2000
	v_mov_b32_e32 v2, s2
.LBB0_651:
	s_or_b64 exec, exec, s[8:9]
	s_waitcnt vmcnt(0)
	s_add_i32 s2, 0, 0x27ff8
	v_mov_b32_e32 v1, 1
	v_mov_b32_e32 v2, s2
	ds_write_b32 v2, v1

; __device__ __forceinline__ unsigned xb_add(unsigned* p, unsigned v) { return __hip_atomic_fetch_add(p, v, __ATOMIC_RELAXED, __HIP_MEMORY_SCOPE_AGENT); }
; template <class Idle>
; __device__ __forceinline__ void xcd_barrier(const XcdBarrier& b, Idle&& idle) {
;     ...
;             __builtin_amdgcn_fence(__ATOMIC_ACQUIRE, "agent");
;             xb_add(&bar[XB_XGEN(b.x)], 1u);
;             asm volatile("s_waitcnt vmcnt(0)" ::: "memory");
;             b.st[2] = 1u;
.LBB0_809:
	s_or_b64 exec, exec, s[6:7]
	s_mov_b64 s[6:7], exec
	v_mbcnt_lo_u32_b32 v1, s6, 0
	v_mbcnt_hi_u32_b32 v1, s7, v1
	v_cmp_eq_u32_e32 vcc, 0, v1
	s_waitcnt vmcnt(0)
	buffer_inv sc1
	s_and_saveexec_b64 s[8:9], vcc
	s_cbranch_execz .LBB0_811
	s_bcnt1_i32_b64 s2, s[6:7]
	v_mov_b32_e32 v1, 0x2000
	v_mov_b32_e32 v2, s2
.LBB0_811:
	s_or_b64 exec, exec, s[8:9]
	s_waitcnt vmcnt(0)
	s_add_i32 s2, 0, 0x27ff8
	v_mov_b32_e32 v1, 1
	v_mov_b32_e32 v2, s2
	ds_write_b32 v2, v1

; __device__ __forceinline__ unsigned xb_add(unsigned* p, unsigned v) { return __hip_atomic_fetch_add(p, v, __ATOMIC_RELAXED, __HIP_MEMORY_SCOPE_AGENT); }
; template <class Idle>
; __device__ __forceinline__ void xcd_barrier(const XcdBarrier& b, Idle&& idle) {
;     ...
;             __builtin_amdgcn_fence(__ATOMIC_ACQUIRE, "agent");
;             xb_add(&bar[XB_XGEN(b.x)], 1u);
;             asm volatile("s_waitcnt vmcnt(0)" ::: "memory");
;             b.st[2] = 1u;
.LBB0_929:
	s_or_b64 exec, exec, s[8:9]
	s_mov_b64 s[8:9], exec
	v_mbcnt_lo_u32_b32 v1, s8, 0
	v_mbcnt_hi_u32_b32 v1, s9, v1
	v_cmp_eq_u32_e32 vcc, 0, v1
	s_waitcnt vmcnt(0)
	buffer_inv sc1
	s_and_saveexec_b64 s[10:11], vcc
	s_cbranch_execz .LBB0_931
	s_bcnt1_i32_b64 s2, s[8:9]
	v_mov_b32_e32 v1, 0x2000
	v_mov_b32_e32 v2, s2
.LBB0_931:
	s_or_b64 exec, exec, s[10:11]
	s_waitcnt vmcnt(0)
	s_add_i32 s2, 0, 0x27ff8
	v_mov_b32_e32 v1, 1
	v_mov_b32_e32 v2, s2
	ds_write_b32 v2, v1

; __device__ __forceinline__ unsigned xb_ld(unsigned* p)              { return __hip_atomic_load(p, __ATOMIC_RELAXED, __HIP_MEMORY_SCOPE_AGENT); }
; #define XB_SPIN(cond, bar) do { unsigned _sp = 0; while (cond) { __builtin_amdgcn_s_sleep(1); \
;     if ((++_sp & 255u) == 0u) { if (xb_ld(&(bar)[XB_TMO])) break; if (_sp > XB_SPIN_CAP) { atomicAdd(&(bar)[XB_TMO], 1u); break; } } } } while (0)
; template <class Idle>
; __device__ __forceinline__ void xcd_barrier(const XcdBarrier& b, Idle&& idle) {
;     ...
;         if (threadIdx.x == 0) {
;             unsigned* bar = b.bar; const unsigned gen = b.st[3];
;             bool rel = xb_ld(&bar[XB_XGEN(b.x)]) != gen;
;             if (!rel && anyw == 0ull) { XB_SPIN(xb_ld(&bar[XB_XGEN(b.x)]) == gen, bar); rel = true; }
;             if (!rel && ++rounds > (1u << 16)) { atomicAdd(&bar[XB_TMO], 1u); rel = true; }
;             if (rel) { __builtin_amdgcn_fence(__ATOMIC_ACQUIRE, "agent"); asm volatile("s_waitcnt vmcnt(0)" ::: "memory"); b.st[2] = 1u; }
.LBB0_986:
	s_lshl_b32 s0, s97, 8
	s_add_u32 s0, s74, s0
	s_addc_u32 s1, s75, 0
	s_add_u32 s0, s74, 0x3500
	s_addc_u32 s1, s75, 0
	s_add_i32 s14, 0, 0x27ffc
	v_mov_b32_e32 v1, 0
	v_mov_b32_e32 v2, 1
	v_mov_b32_e32 v3, s3
	s_branch .LBB0_990

; __device__ __forceinline__ unsigned xb_add(unsigned* p, unsigned v) { return __hip_atomic_fetch_add(p, v, __ATOMIC_RELAXED, __HIP_MEMORY_SCOPE_AGENT); }
; template <class Idle>
; __device__ __forceinline__ void xcd_barrier(const XcdBarrier& b, Idle&& idle) {
;     ...
;             __builtin_amdgcn_fence(__ATOMIC_ACQUIRE, "agent");
;             xb_add(&bar[XB_XGEN(b.x)], 1u);
;             asm volatile("s_waitcnt vmcnt(0)" ::: "memory");
;             b.st[2] = 1u;
.LBB0_1030:
	s_or_b64 exec, exec, s[6:7]
	s_mov_b64 s[6:7], exec
	v_mbcnt_lo_u32_b32 v1, s6, 0
	v_mbcnt_hi_u32_b32 v1, s7, v1
	v_cmp_eq_u32_e32 vcc, 0, v1
	s_waitcnt vmcnt(0)
	buffer_inv sc1
	s_and_saveexec_b64 s[8:9], vcc
	s_cbranch_execz .LBB0_1032
	s_bcnt1_i32_b64 s2, s[6:7]
	v_mov_b32_e32 v1, 0x2000
	v_mov_b32_e32 v2, s2
.LBB0_1032:
	s_or_b64 exec, exec, s[8:9]
	s_waitcnt vmcnt(0)
	s_add_i32 s2, 0, 0x27ff8
	v_mov_b32_e32 v1, 1
	v_mov_b32_e32 v2, s2
	ds_write_b32 v2, v1
